# placement flag remembered in an LDS word after the first XCD-local barrier: the P7->P8 seam makes no global round trip
# baseline (speedup 1.0000x reference)
.Lxl_spin_0:
	global_load_dword v6, v5, s[10:11] offset:1024 sc1
	s_waitcnt vmcnt(0)
	v_cmp_ne_u32_e32 vcc, 0, v2
	s_cbranch_vccnz .Lxl_full_0
	v_mov_b32_e32 v7, 0x20168
	v_mov_b32_e32 v3, 1
	ds_write_b32 v7, v3
	v_cmp_ge_u32_e32 vcc, v6, v4
	s_cbranch_vccnz .LBB0_950
	s_sleep 1
	s_add_u32 s6, s6, 1
	s_cmp_lt_u32 s6, 0x40000
	s_cbranch_scc1 .Lxl_spin_0
	s_branch .LBB0_950

.LBB0_1232:
	s_cmp_gt_i32 s81, 8
	s_cselect_b64 s[0:1], -1, 0
	s_and_b64 s[2:3], s[12:13], s[0:1]
	s_andn2_b64 vcc, exec, s[2:3]
	s_cbranch_vccnz .LBB0_1284
	s_waitcnt vmcnt(0)
	s_waitcnt vmcnt(0) lgkmcnt(0)
	v_readlane_b32 s6, v255, 9
	v_readlane_b32 s7, v255, 10
	v_readlane_b32 s9, v255, 8
	v_readlane_b32 s14, v255, 18
	s_lshl_b32 s8, s9, 5
	s_lshl_b32 s14, s14, 2
	s_add_i32 s8, s8, s14
	s_add_i32 s8, s8, 0x4000
	s_mov_b64 s[16:17], exec
	s_mov_b64 exec, 1
	v_mov_b32_e32 v2, s8
	v_mov_b32_e32 v4, 1
	global_atomic_add v2, v4, s[6:7]
	s_mov_b64 exec, s[16:17]
	s_barrier
	s_mov_b64 s[4:5], exec
	v_readlane_b32 s2, v255, 12
	v_readlane_b32 s3, v255, 13
	s_and_b64 s[2:3], s[4:5], s[2:3]
	s_mov_b64 exec, s[2:3]
	s_cbranch_execz .LBB0_1283
	v_mov_b32_e32 v2, 0x20168
	ds_read_b32 v2, v2
	s_waitcnt lgkmcnt(0)
	v_cmp_eq_u32_e32 vcc, 1, v2
	s_cbranch_vccz .Lxl_slow_2
	buffer_inv sc1
	s_branch .LBB0_1283
.Lxl_slow_2:
	v_readlane_b32 s8, v255, 11
	v_readlane_b32 s12, v255, 9
	v_readlane_b32 s13, v255, 10
	v_mov_b32_e32 v4, 0x20160
	ds_read_b32 v4, v4
	s_lshl_b32 s8, s8, 8
	s_add_u32 s8, s12, s8
	s_addc_u32 s9, s13, 0
	v_mov_b32_e32 v5, 0x2000
	v_mov_b32_e32 v6, 1
	v_mov_b32_e32 v2, 0x3000
	s_mov_b32 s2, 0
	global_atomic_add v5, v6, s[8:9] offset:1024
	buffer_inv sc1
	global_load_dword v2, v2, s[12:13] offset:896 sc1
	s_waitcnt lgkmcnt(0)
	v_mul_u32_u24_e32 v4, 3, v4
